# W2 conversion items split asymmetrically: workgroups that ran one G4 unit fewer take more conversion items
# baseline (speedup 1.0000x reference)
; #define LAS __attribute__((address_space(3)))
; DI void transpose_item(const float* W, int K, int N, bf16_t* WT, int mode, LAS float* scr, int item, int lane) {
;     ...
;     { const int rr = lane >> 3, c4 = lane & 7; f32x4 v[8];
; #pragma unroll
;       for (int i = 0; i < 8; ++i) v[i] = *(const f32x4*)(W + (size_t)(k0 + 8 * i + rr) * N + n0 + 4 * c4);
; #pragma unroll
;       for (int i = 0; i < 8; ++i) { LAS float* d = scr + (8 * i + rr) * 33 + 4 * c4; d[0] = v[i].x; d[1] = v[i].y; d[2] = v[i].z; d[3] = v[i].w; } }
; DI void phase_expert_weights(const Frame& F, int l, int which) {
;     ...
;         constexpr int IPM = (FF / 64) * (D / 32);
;         for (int it = F.gw; it < NE * IPM; it += F.NGW) { const int mtx = l * NE + it / IPM, r = it % IPM;
;             transpose_item(F.ap->in[34] + (size_t)mtx * FF * D, FF, D, (bf16_t*)(ws + WS_W2 + (size_t)mtx * D * FF), 2, scr, r, F.lane); }
.LBB0_1248:
	s_ashr_i32 s7, s7, 6
	s_lshl_b32 s6, s6, 3
	s_add_i32 s6, s6, s7
	s_lshl_b32 s67, s2, 3
	s_movk_i32 s66, 0x4000
	v_readlane_b32 s68, v253, 38
	s_nop 3
	v_mov_b32_e32 v2, s68
	ds_read_b32 v2, v2
	s_waitcnt lgkmcnt(0)
	v_readfirstlane_b32 s68, v2
	s_nop 3
	s_lshl_b32 s68, s68, 3
	s_and_b32 s68, s68, 0xff
	s_cmp_gt_u32 s68, 0xc0
	s_cbranch_scc1 .Lw2_go
	s_cmp_eq_u32 s2, 0x100
	s_cbranch_scc0 .Lw2_go
	s_cmp_lt_u32 s94, s68
	s_cbranch_scc1 .Lw2_late
	s_sub_i32 s69, s94, s68
	s_lshl_b32 s69, s69, 3
	s_add_i32 s69, s69, s7
	s_mul_i32 s6, s68, 48
	s_add_i32 s6, s6, s69
	s_sub_i32 s67, 0x100, s68
	s_lshl_b32 s67, s67, 3
	s_branch .Lw2_go
.Lw2_late:
	s_mul_i32 s6, s94, 48
	s_mul_i32 s69, s7, 6
	s_add_i32 s6, s6, s69
	s_mov_b32 s67, 1
	s_add_i32 s66, s6, 6
.Lw2_go:
	s_cmp_ge_i32 s6, s66
	s_cbranch_scc1 .LBB0_1251
	s_load_dwordx2 s[8:9], s[4:5], 0x128
	s_load_dwordx2 s[38:39], s[4:5], 0x110
	s_mov_b32 s4, s67
	s_lshl_b32 s2, s7, 14
	s_add_i32 s2, s2, 0
	v_bfe_u32 v30, v0, 3, 3
	v_and_b32_e32 v1, 7, v0
	s_waitcnt lgkmcnt(0)
	s_add_u32 s5, s8, 0x24000000
	v_lshlrev_b32_e32 v0, 2, v1
	v_lshl_add_u32 v2, v1, 4, s2
	v_mul_u32_u24_e32 v3, 0x84, v30
	v_lshlrev_b32_e32 v28, 3, v1
	v_mul_u32_u24_e32 v1, 0x420, v1
	v_lshlrev_b32_e32 v4, 2, v30
	s_addc_u32 s7, s9, 0
	v_or_b32_e32 v31, 8, v30
	v_or_b32_e32 v32, 16, v30
	v_or_b32_e32 v33, 24, v30
	v_mov_b32_e32 v29, v193
	v_add3_u32 v34, s2, v1, v4
	v_lshlrev_b32_e32 v192, 2, v0
	v_add_u32_e32 v35, v2, v3
.LBB0_1250:
	s_ashr_i32 s2, s6, 31
	s_lshr_b32 s2, s2, 23
	s_add_i32 s2, s6, s2
	s_ashr_i32 s8, s2, 9
	s_add_i32 s8, s8, s28
	s_and_b32 s2, s2, 0xfe00
	s_ashr_i32 s9, s8, 31
	s_sub_i32 s2, s6, s2
	s_lshl_b64 s[12:13], s[8:9], 20
	s_lshl_b64 s[8:9], s[8:9], 22
	s_add_u32 s17, s38, s8
	s_addc_u32 s19, s39, s9
	s_add_u32 s8, s5, s12
	s_sext_i32_i16 s10, s2
	s_addc_u32 s9, s7, s13
	s_bfe_u32 s10, s10, 0x5001a
	s_add_i32 s10, s2, s10
	s_sext_i32_i16 s12, s10
	s_and_b32 s10, s10, 0xffe0
	s_sub_i32 s2, s2, s10
	s_sext_i32_i16 s2, s2
	s_lshl_b32 s42, s2, 5
	s_lshl_b32 s10, s12, 1
	s_ashr_i32 s43, s42, 31
	s_andn2_b32 s10, s10, 63
	s_lshl_b64 s[12:13], s[42:43], 2
	v_or_b32_e32 v0, s10, v30
	s_add_u32 s12, s17, s12
	s_addc_u32 s13, s19, s13
	v_ashrrev_i32_e32 v1, 31, v0
	v_lshl_add_u64 v[2:3], s[12:13], 0, v[192:193]
	v_lshlrev_b64 v[4:5], 12, v[0:1]
	v_lshl_add_u64 v[4:5], v[2:3], 0, v[4:5]
	global_load_dwordx4 v[36:39], v[4:5], off
	v_or_b32_e32 v4, 8, v0
	v_ashrrev_i32_e32 v5, 31, v4
	v_lshlrev_b64 v[4:5], 12, v[4:5]
	v_lshl_add_u64 v[4:5], v[2:3], 0, v[4:5]
	global_load_dwordx4 v[24:27], v[4:5], off
	v_or_b32_e32 v4, 16, v0
	v_ashrrev_i32_e32 v5, 31, v4
	v_lshlrev_b64 v[4:5], 12, v[4:5]
	v_lshl_add_u64 v[4:5], v[2:3], 0, v[4:5]
	global_load_dwordx4 v[20:23], v[4:5], off
	v_or_b32_e32 v4, 24, v0
	v_ashrrev_i32_e32 v5, 31, v4
	v_lshlrev_b64 v[4:5], 12, v[4:5]
	v_lshl_add_u64 v[4:5], v[2:3], 0, v[4:5]
	global_load_dwordx4 v[16:19], v[4:5], off
	v_or_b32_e32 v4, 32, v0
	v_ashrrev_i32_e32 v5, 31, v4
	v_lshlrev_b64 v[4:5], 12, v[4:5]
	v_lshl_add_u64 v[4:5], v[2:3], 0, v[4:5]
	global_load_dwordx4 v[12:15], v[4:5], off
	v_or_b32_e32 v4, 40, v0
	v_ashrrev_i32_e32 v5, 31, v4
	v_lshlrev_b64 v[4:5], 12, v[4:5]
	v_lshl_add_u64 v[4:5], v[2:3], 0, v[4:5]
	global_load_dwordx4 v[8:11], v[4:5], off
	v_or_b32_e32 v4, 48, v0
	v_ashrrev_i32_e32 v5, 31, v4
	v_lshlrev_b64 v[4:5], 12, v[4:5]
	v_or_b32_e32 v0, 56, v0
	v_lshl_add_u64 v[4:5], v[2:3], 0, v[4:5]
	v_ashrrev_i32_e32 v1, 31, v0
	global_load_dwordx4 v[4:7], v[4:5], off
	v_lshlrev_b64 v[0:1], 12, v[0:1]
	v_lshl_add_u64 v[0:1], v[2:3], 0, v[0:1]
	global_load_dwordx4 v[0:3], v[0:1], off
	s_ashr_i32 s2, s10, 31
	s_add_u32 s8, s8, s10
	s_addc_u32 s9, s9, s2
	s_add_i32 s6, s6, s4
	s_cmp_lt_i32 s6, s66
	s_waitcnt vmcnt(0)
	ds_write2_b32 v35, v36, v37 offset1:1
	ds_write2_b32 v35, v38, v39 offset0:2 offset1:3
	v_add_u32_e32 v36, 0x420, v35
	ds_write2_b32 v36, v24, v25 offset1:1
	v_add_u32_e32 v24, 0x428, v35
	ds_write2_b32 v24, v26, v27 offset1:1
	v_add_u32_e32 v24, 0x840, v35
	ds_write2_b32 v24, v20, v21 offset1:1
	v_add_u32_e32 v20, 0x848, v35
	ds_write2_b32 v20, v22, v23 offset1:1
	v_add_u32_e32 v20, 0xc60, v35
	ds_write2_b32 v20, v16, v17 offset1:1
	v_add_u32_e32 v16, 0xc68, v35
	ds_write2_b32 v16, v18, v19 offset1:1
	v_add_u32_e32 v16, 0x1080, v35
	ds_write2_b32 v16, v12, v13 offset1:1
	v_add_u32_e32 v12, 0x1088, v35
	ds_write2_b32 v12, v14, v15 offset1:1
	v_add_u32_e32 v12, 0x14a0, v35
	v_mov_b32_e32 v13, v193
	ds_write2_b32 v12, v8, v9 offset1:1
	v_add_u32_e32 v8, 0x14a8, v35
	ds_write2_b32 v8, v10, v11 offset1:1
	v_add_u32_e32 v8, 0x18c0, v35
	v_mov_b32_e32 v12, v193
	ds_write2_b32 v8, v4, v5 offset1:1
	v_add_u32_e32 v4, 0x18c8, v35
	ds_write2_b32 v4, v6, v7 offset1:1
	v_add_u32_e32 v4, 0x1ce0, v35
	ds_write2_b32 v4, v0, v1 offset1:1
	v_add_u32_e32 v0, 0x1ce8, v35
	ds_write2_b32 v0, v2, v3 offset1:1
	s_waitcnt lgkmcnt(0)
; #define LAS __attribute__((address_space(3)))
; DI unsigned pk2(float lo, float hi) { return f2bf(lo) | (f2bf(hi) << 16); }
; DI unsigned pk_fp8x4(float a, float b, float c, float d) { int p = 0; p = __builtin_amdgcn_cvt_pk_fp8_f32(a, b, p, false); p = __builtin_amdgcn_cvt_pk_fp8_f32(c, d, p, true); return (unsigned)p; }
; #define LDS_WAIT() asm volatile("s_waitcnt lgkmcnt(0)" ::: "memory")
; DI void transpose_item(const float* W, int K, int N, bf16_t* WT, int mode, LAS float* scr, int item, int lane) {
;     ...
;     LDS_WAIT(); asm volatile("" ::: "memory");
;     const int c = lane & 7;
; #pragma unroll
;     for (int j = 0; j < 4; ++j) { const int n = (lane >> 3) + 8 * j; const LAS float* s = scr + (8 * c) * 33 + n;
;         const int row = (mode & 1) ? w1_row(n0 + n) : (n0 + n);
;         if (mode & 2) { u32x2 o; o.x = pk_fp8x4(s[0 * 33] * W8_SCALE, s[1 * 33] * W8_SCALE, s[2 * 33] * W8_SCALE, s[3 * 33] * W8_SCALE); o.y = pk_fp8x4(s[4 * 33] * W8_SCALE, s[5 * 33] * W8_SCALE, s[6 * 33] * W8_SCALE, s[7 * 33] * W8_SCALE);
;             *(u32x2*)((unsigned char*)WT + (size_t)row * K + k0 + 8 * c) = o; }
;         else { u32x4 o; o.x = pk2(s[0 * 33], s[1 * 33]); o.y = pk2(s[2 * 33], s[3 * 33]); o.z = pk2(s[4 * 33], s[5 * 33]); o.w = pk2(s[6 * 33], s[7 * 33]);
;             *(u32x4*)(WT + (size_t)row * K + k0 + 8 * c) = o; } }
;     LDS_WAIT(); asm volatile("" ::: "memory");
	ds_read2_b32 v[4:5], v34 offset1:8
	ds_read2_b32 v[6:7], v34 offset0:33 offset1:41
	ds_read2_b32 v[14:15], v34 offset0:132 offset1:140
	ds_read2_b32 v[16:17], v34 offset0:165 offset1:173
	ds_read2_b32 v[8:9], v34 offset0:66 offset1:74
	ds_read2_b32 v[10:11], v34 offset0:99 offset1:107
	s_waitcnt lgkmcnt(5)
	v_mul_f32_e32 v3, 0x42800000, v4
	s_waitcnt lgkmcnt(4)
	v_mul_f32_e32 v4, 0x42800000, v6
	ds_read2_b32 v[18:19], v34 offset0:198 offset1:206
	ds_read2_b32 v[20:21], v34 offset0:231 offset1:239
	v_cvt_pk_fp8_f32 v12, v3, v4
	s_waitcnt lgkmcnt(5)
	v_mul_f32_e32 v3, 0x42800000, v14
	s_waitcnt lgkmcnt(4)
	v_mul_f32_e32 v4, 0x42800000, v16
	v_cvt_pk_fp8_f32 v13, v3, v4
	s_waitcnt lgkmcnt(3)
	v_mul_f32_e32 v6, 0x42800000, v8
	s_waitcnt lgkmcnt(2)
	v_mul_f32_e32 v8, 0x42800000, v10
	v_cvt_pk_fp8_f32 v12, v6, v8 op_sel:[0,0,1]
	s_waitcnt lgkmcnt(1)
	v_mul_f32_e32 v6, 0x42800000, v18
	s_waitcnt lgkmcnt(0)
	v_mul_f32_e32 v8, 0x42800000, v20
	v_or_b32_e32 v2, s42, v30
	v_cvt_pk_fp8_f32 v13, v6, v8 op_sel:[0,0,1]
	v_ashrrev_i32_e32 v3, 31, v2
	v_lshl_add_u64 v[0:1], s[8:9], 0, v[28:29]
	v_lshlrev_b64 v[2:3], 10, v[2:3]
	v_lshl_add_u64 v[2:3], v[0:1], 0, v[2:3]
	global_store_dwordx2 v[2:3], v[12:13], off
	v_mul_f32_e32 v3, 0x42800000, v5
	v_mul_f32_e32 v5, 0x42800000, v7
	v_mov_b32_e32 v4, v193
	v_cvt_pk_fp8_f32 v4, v3, v5
	v_mul_f32_e32 v6, 0x42800000, v9
	v_mul_f32_e32 v7, 0x42800000, v11
	v_mul_f32_e32 v3, 0x42800000, v15
	v_cvt_pk_fp8_f32 v4, v6, v7 op_sel:[0,0,1]
	v_mul_f32_e32 v6, 0x42800000, v17
	v_mov_b32_e32 v5, v193
	v_cvt_pk_fp8_f32 v5, v3, v6
	v_mul_f32_e32 v7, 0x42800000, v19
	v_mul_f32_e32 v8, 0x42800000, v21
	v_or_b32_e32 v2, s42, v31
	v_cvt_pk_fp8_f32 v5, v7, v8 op_sel:[0,0,1]
	v_ashrrev_i32_e32 v3, 31, v2
	v_lshlrev_b64 v[2:3], 10, v[2:3]
	v_lshl_add_u64 v[2:3], v[0:1], 0, v[2:3]
	global_store_dwordx2 v[2:3], v[4:5], off
	ds_read2_b32 v[4:5], v34 offset0:16 offset1:24
	ds_read2_b32 v[6:7], v34 offset0:49 offset1:57
	ds_read2_b32 v[14:15], v34 offset0:148 offset1:156
	ds_read2_b32 v[16:17], v34 offset0:181 offset1:189
	ds_read2_b32 v[8:9], v34 offset0:82 offset1:90
	ds_read2_b32 v[10:11], v34 offset0:115 offset1:123
	s_waitcnt lgkmcnt(5)
	v_mul_f32_e32 v3, 0x42800000, v4
	s_waitcnt lgkmcnt(4)
	v_mul_f32_e32 v4, 0x42800000, v6
	v_mov_b32_e32 v12, v193
	ds_read2_b32 v[18:19], v34 offset0:214 offset1:222
	ds_read2_b32 v[20:21], v34 offset0:247 offset1:255
	v_cvt_pk_fp8_f32 v12, v3, v4
	s_waitcnt lgkmcnt(5)
	v_mul_f32_e32 v3, 0x42800000, v14
	s_waitcnt lgkmcnt(4)
	v_mul_f32_e32 v4, 0x42800000, v16
	v_mov_b32_e32 v13, v193
	v_cvt_pk_fp8_f32 v13, v3, v4
	s_waitcnt lgkmcnt(3)
	v_mul_f32_e32 v6, 0x42800000, v8
	s_waitcnt lgkmcnt(2)
	v_mul_f32_e32 v8, 0x42800000, v10
	v_cvt_pk_fp8_f32 v12, v6, v8 op_sel:[0,0,1]
	s_waitcnt lgkmcnt(1)
	v_mul_f32_e32 v6, 0x42800000, v18
	s_waitcnt lgkmcnt(0)
	v_mul_f32_e32 v8, 0x42800000, v20
	v_or_b32_e32 v2, s42, v32
	v_cvt_pk_fp8_f32 v13, v6, v8 op_sel:[0,0,1]
	v_ashrrev_i32_e32 v3, 31, v2
	v_lshlrev_b64 v[2:3], 10, v[2:3]
	v_lshl_add_u64 v[2:3], v[0:1], 0, v[2:3]
	global_store_dwordx2 v[2:3], v[12:13], off
	v_mul_f32_e32 v3, 0x42800000, v5
	v_mul_f32_e32 v5, 0x42800000, v7
	v_mov_b32_e32 v2, v193
	v_cvt_pk_fp8_f32 v2, v3, v5
	v_mul_f32_e32 v6, 0x42800000, v9
	v_mul_f32_e32 v7, 0x42800000, v11
	v_mul_f32_e32 v5, 0x42800000, v15
	v_cvt_pk_fp8_f32 v2, v6, v7 op_sel:[0,0,1]
	v_mul_f32_e32 v6, 0x42800000, v17
	v_mov_b32_e32 v3, v193
	v_cvt_pk_fp8_f32 v3, v5, v6
	v_mul_f32_e32 v7, 0x42800000, v19
	v_mul_f32_e32 v8, 0x42800000, v21
	v_or_b32_e32 v4, s42, v33
	v_cvt_pk_fp8_f32 v3, v7, v8 op_sel:[0,0,1]
	v_ashrrev_i32_e32 v5, 31, v4
	v_lshlrev_b64 v[4:5], 10, v[4:5]
	v_lshl_add_u64 v[0:1], v[0:1], 0, v[4:5]
	global_store_dwordx2 v[0:1], v[2:3], off
	s_waitcnt lgkmcnt(0)
	s_cbranch_scc1 .LBB0_1250
